# baseline (speedup 1.0000x reference)
.LBB1_2:
	s_or_b64 exec, exec, s[2:3]
	v_and_b32_e32 v52, 3, v52
	v_and_b32_e32 v54, 48, v0
	v_lshlrev_b32_e32 v55, 2, v0
	v_lshl_or_b32 v54, v50, 6, v54
	v_and_b32_e32 v55, 32, v55
	v_lshlrev_b32_e32 v56, 14, v53
	v_lshlrev_b32_e32 v57, 13, v52
	v_lshl_or_b32 v52, v52, 6, s20
	v_lshlrev_b32_e32 v51, 2, v51
	s_movk_i32 s2, 0x4c
	v_bitop3_b32 v191, v54, v57, v55 bitop3:0xde
	v_bitop3_b32 v192, v54, v56, v55 bitop3:0xde
	v_or_b32_e32 v54, v52, v51
	v_bitop3_b32 v51, v52, s2, v51 bitop3:0xc8
	v_lshrrev_b32_e32 v52, 6, v52
	s_lshl_b32 s2, s19, 2
	v_and_or_b32 v52, v52, 14, s18
	v_lshlrev_b32_e32 v182, 2, v51
	v_mov_b32_e32 v183, 0
	s_add_u32 s2, s8, s2
	v_lshlrev_b32_e32 v52, 14, v52
	v_lshlrev_b32_e32 v53, 7, v53
	v_lshl_add_u64 v[184:185], s[10:11], 0, v[182:183]
	s_addc_u32 s3, s9, 0
	v_lshlrev_b32_e32 v182, 2, v54
	v_or3_b32 v193, v53, v52, v50
	s_mov_b32 s18, 0
	v_lshl_add_u64 v[186:187], s[2:3], 0, v[182:183]
	global_load_dwordx4 v[240:243], v[186:187], off
	global_load_dwordx4 v[244:247], v[186:187], off offset:64
	global_load_dwordx4 v[248:251], v[186:187], off offset:128
	global_load_dwordx4 v[252:255], v[186:187], off offset:192
	s_mov_b32 s2, s6
	s_mov_b32 s3, s7
	s_movk_i32 s8, 0x2000
	s_movk_i32 s9, 0x6000
	s_mov_b32 s10, 0xa000
	s_mov_b32 s11, 0xe000
	s_mov_b32 s19, 0
	s_mov_b32 s20, 0
	v_mov_b32_e32 v50, v183
	v_mov_b32_e32 v51, v183
	v_mov_b32_e32 v52, v183
	v_mov_b32_e32 v53, v183
	v_mov_b32_e32 v58, v183
	v_mov_b32_e32 v59, v183
	v_mov_b32_e32 v60, v183
	v_mov_b32_e32 v61, v183
	v_mov_b32_e32 v66, v183
	v_mov_b32_e32 v67, v183
	v_mov_b32_e32 v68, v183
	v_mov_b32_e32 v69, v183
	v_mov_b32_e32 v78, v183
	v_mov_b32_e32 v79, v183
	v_mov_b32_e32 v80, v183
	v_mov_b32_e32 v81, v183
	v_mov_b32_e32 v54, v183
	v_mov_b32_e32 v55, v183
	v_mov_b32_e32 v56, v183
	v_mov_b32_e32 v57, v183
	v_mov_b32_e32 v70, v183
	v_mov_b32_e32 v71, v183
	v_mov_b32_e32 v72, v183
	v_mov_b32_e32 v73, v183
	v_mov_b32_e32 v86, v183
	v_mov_b32_e32 v87, v183
	v_mov_b32_e32 v88, v183
	v_mov_b32_e32 v89, v183
	v_mov_b32_e32 v94, v183
	v_mov_b32_e32 v95, v183
	v_mov_b32_e32 v96, v183
	v_mov_b32_e32 v97, v183
	v_mov_b32_e32 v62, v183
	v_mov_b32_e32 v63, v183
	v_mov_b32_e32 v64, v183
	v_mov_b32_e32 v65, v183
	v_mov_b32_e32 v82, v183
	v_mov_b32_e32 v83, v183
	v_mov_b32_e32 v84, v183
	v_mov_b32_e32 v85, v183
	v_mov_b32_e32 v102, v183
	v_mov_b32_e32 v103, v183
	v_mov_b32_e32 v104, v183
	v_mov_b32_e32 v105, v183
	v_mov_b32_e32 v110, v183
	v_mov_b32_e32 v111, v183
	v_mov_b32_e32 v112, v183
	v_mov_b32_e32 v113, v183
	v_mov_b32_e32 v74, v183
	v_mov_b32_e32 v75, v183
	v_mov_b32_e32 v76, v183
	v_mov_b32_e32 v77, v183
	v_mov_b32_e32 v98, v183
	v_mov_b32_e32 v99, v183
	v_mov_b32_e32 v100, v183
	v_mov_b32_e32 v101, v183
	v_mov_b32_e32 v118, v183
	v_mov_b32_e32 v119, v183
	v_mov_b32_e32 v120, v183
	v_mov_b32_e32 v121, v183
	v_mov_b32_e32 v126, v183
	v_mov_b32_e32 v127, v183
	v_mov_b32_e32 v128, v183
	v_mov_b32_e32 v129, v183
	v_mov_b32_e32 v90, v183
	v_mov_b32_e32 v91, v183
	v_mov_b32_e32 v92, v183
	v_mov_b32_e32 v93, v183
	v_mov_b32_e32 v114, v183
	v_mov_b32_e32 v115, v183
	v_mov_b32_e32 v116, v183
	v_mov_b32_e32 v117, v183
	v_mov_b32_e32 v134, v183
	v_mov_b32_e32 v135, v183
	v_mov_b32_e32 v136, v183
	v_mov_b32_e32 v137, v183
	v_mov_b32_e32 v138, v183
	v_mov_b32_e32 v139, v183
	v_mov_b32_e32 v140, v183
	v_mov_b32_e32 v141, v183
	v_mov_b32_e32 v106, v183
	v_mov_b32_e32 v107, v183
	v_mov_b32_e32 v108, v183
	v_mov_b32_e32 v109, v183
	v_mov_b32_e32 v130, v183
	v_mov_b32_e32 v131, v183
	v_mov_b32_e32 v132, v183
	v_mov_b32_e32 v133, v183
	v_mov_b32_e32 v150, v183
	v_mov_b32_e32 v151, v183
	v_mov_b32_e32 v152, v183
	v_mov_b32_e32 v153, v183
	v_mov_b32_e32 v154, v183
	v_mov_b32_e32 v155, v183
	v_mov_b32_e32 v156, v183
	v_mov_b32_e32 v157, v183
	v_mov_b32_e32 v122, v183
	v_mov_b32_e32 v123, v183
	v_mov_b32_e32 v124, v183
	v_mov_b32_e32 v125, v183
	v_mov_b32_e32 v146, v183
	v_mov_b32_e32 v147, v183
	v_mov_b32_e32 v148, v183
	v_mov_b32_e32 v149, v183
	v_mov_b32_e32 v162, v183
	v_mov_b32_e32 v163, v183
	v_mov_b32_e32 v164, v183
	v_mov_b32_e32 v165, v183
	v_mov_b32_e32 v166, v183
	v_mov_b32_e32 v167, v183
	v_mov_b32_e32 v168, v183
	v_mov_b32_e32 v169, v183
	v_mov_b32_e32 v142, v183
	v_mov_b32_e32 v143, v183
	v_mov_b32_e32 v144, v183
	v_mov_b32_e32 v145, v183
	v_mov_b32_e32 v158, v183
	v_mov_b32_e32 v159, v183
	v_mov_b32_e32 v160, v183
	v_mov_b32_e32 v161, v183
	v_mov_b32_e32 v170, v183
	v_mov_b32_e32 v171, v183
	v_mov_b32_e32 v172, v183
	v_mov_b32_e32 v173, v183
	v_mov_b32_e32 v174, v183
	v_mov_b32_e32 v175, v183
	v_mov_b32_e32 v176, v183
	v_mov_b32_e32 v177, v183
	s_branch .LBB1_4

.LBB1_4:
	v_add_u32_e32 v182, s19, v191
	v_add_u32_e32 v238, s19, v192
	ds_read_b128 v[178:181], v182 offset:32768
	ds_read_b128 v[194:197], v182 offset:34816
	ds_read_b128 v[198:201], v182 offset:36864
	ds_read_b128 v[202:205], v182 offset:38912
	ds_read_b128 v[206:209], v238
	ds_read_b128 v[210:213], v238 offset:2048
	ds_read_b128 v[214:217], v238 offset:4096
	ds_read_b128 v[218:221], v238 offset:6144
	ds_read_b128 v[222:225], v238 offset:8192
	ds_read_b128 v[226:229], v238 offset:10240
	ds_read_b128 v[230:233], v238 offset:12288
	ds_read_b128 v[234:237], v238 offset:14336
	s_min_u32 s21, s20, 29
	s_xor_b32 s19, s19, 0x10000
	v_add_u32_e32 v239, s19, v189
	s_waitcnt vmcnt(11)
	v_cvt_pk_bf16_f32 v13, v12, v13
	v_cvt_pk_bf16_f32 v12, v10, v11
	s_waitcnt vmcnt(10)
	v_cvt_pk_bf16_f32 v11, v20, v21
	v_cvt_pk_bf16_f32 v10, v18, v19
	ds_write2st64_b64 v239, v[12:13], v[10:11] offset1:8
	s_waitcnt vmcnt(9)
	v_cvt_pk_bf16_f32 v11, v24, v25
	v_cvt_pk_bf16_f32 v10, v22, v23
	s_waitcnt vmcnt(8)
	v_cvt_pk_bf16_f32 v13, v32, v33
	v_cvt_pk_bf16_f32 v12, v30, v31
	ds_write2st64_b64 v239, v[10:11], v[12:13] offset0:16 offset1:24
	s_waitcnt vmcnt(7)
	v_cvt_pk_bf16_f32 v11, v36, v37
	v_cvt_pk_bf16_f32 v10, v34, v35
	s_waitcnt vmcnt(6)
	v_cvt_pk_bf16_f32 v13, v40, v41
	v_cvt_pk_bf16_f32 v12, v38, v39
	ds_write2st64_b64 v239, v[10:11], v[12:13] offset0:32 offset1:40
	s_waitcnt vmcnt(5)
	v_cvt_pk_bf16_f32 v11, v44, v45
	v_cvt_pk_bf16_f32 v10, v42, v43
	s_waitcnt vmcnt(4)
	v_cvt_pk_bf16_f32 v13, v48, v49
	v_cvt_pk_bf16_f32 v12, v46, v47
	ds_write2st64_b64 v239, v[10:11], v[12:13] offset0:48 offset1:56
	s_waitcnt lgkmcnt(0)
	s_add_i32 s21, s21, 2
	s_barrier
	s_setprio 1
	s_lshl_b32 s22, s21, 1
	s_and_b32 s22, s22, 0x60
	s_add_i32 s22, s22, s12
	s_lshl_b32 s22, s22, 6
	s_and_b32 s22, s22, 0x3f00
	s_or_b32 s22, s22, s13
	s_lshl_b32 s23, s21, 23
	s_lshl_b32 s22, s22, 9
	s_and_b32 s23, s23, 0x7000000
	s_or_b32 s22, s22, s23
	s_lshl_b32 s23, s21, 8
	s_and_b32 s23, s23, 0x100
	s_or_b32 s22, s22, s23
	s_or_b32 s23, s22, 0x4000
	s_waitcnt lgkmcnt(11)
	v_mfma_f32_16x16x32_bf16 v[174:177], v[178:181], v[206:209], v[174:177]
	v_mfma_f32_16x16x32_bf16 v[170:173], v[194:197], v[206:209], v[170:173]
	v_mfma_f32_16x16x32_bf16 v[158:161], v[198:201], v[206:209], v[158:161]
	buffer_load_dwordx4 v[10:13], v1, s[4:7], s22 offen sc0 nt
	v_mfma_f32_16x16x32_bf16 v[142:145], v[202:205], v[206:209], v[142:145]
	s_waitcnt lgkmcnt(10)
	v_mfma_f32_16x16x32_bf16 v[166:169], v[178:181], v[210:213], v[166:169]
	v_mfma_f32_16x16x32_bf16 v[162:165], v[194:197], v[210:213], v[162:165]
	v_mfma_f32_16x16x32_bf16 v[146:149], v[198:201], v[210:213], v[146:149]
	buffer_load_dwordx4 v[18:21], v1, s[4:7], s23 offen sc0 nt
	s_or_b32 s23, s22, 0x8000
	v_mfma_f32_16x16x32_bf16 v[122:125], v[202:205], v[210:213], v[122:125]
	s_waitcnt lgkmcnt(9)
	v_mfma_f32_16x16x32_bf16 v[154:157], v[178:181], v[214:217], v[154:157]
	v_mfma_f32_16x16x32_bf16 v[150:153], v[194:197], v[214:217], v[150:153]
	v_mfma_f32_16x16x32_bf16 v[130:133], v[198:201], v[214:217], v[130:133]
	buffer_load_dwordx4 v[22:25], v1, s[4:7], s23 offen sc0 nt
	s_or_b32 s23, s22, 0xc000
	v_mfma_f32_16x16x32_bf16 v[106:109], v[202:205], v[214:217], v[106:109]
	s_waitcnt lgkmcnt(8)
	v_mfma_f32_16x16x32_bf16 v[138:141], v[178:181], v[218:221], v[138:141]
	v_mfma_f32_16x16x32_bf16 v[134:137], v[194:197], v[218:221], v[134:137]
	v_mfma_f32_16x16x32_bf16 v[114:117], v[198:201], v[218:221], v[114:117]
	buffer_load_dwordx4 v[30:33], v1, s[4:7], s23 offen sc0 nt
	s_or_b32 s23, s22, 0x10000
	v_mfma_f32_16x16x32_bf16 v[90:93], v[202:205], v[218:221], v[90:93]
	s_waitcnt lgkmcnt(7)
	v_mfma_f32_16x16x32_bf16 v[126:129], v[178:181], v[222:225], v[126:129]
	v_mfma_f32_16x16x32_bf16 v[118:121], v[194:197], v[222:225], v[118:121]
	v_mfma_f32_16x16x32_bf16 v[98:101], v[198:201], v[222:225], v[98:101]
	buffer_load_dwordx4 v[34:37], v1, s[4:7], s23 offen sc0 nt
	s_or_b32 s23, s22, 0x14000
	v_mfma_f32_16x16x32_bf16 v[74:77], v[202:205], v[222:225], v[74:77]
	s_waitcnt lgkmcnt(6)
	v_mfma_f32_16x16x32_bf16 v[110:113], v[178:181], v[226:229], v[110:113]
	v_mfma_f32_16x16x32_bf16 v[102:105], v[194:197], v[226:229], v[102:105]
	v_mfma_f32_16x16x32_bf16 v[82:85], v[198:201], v[226:229], v[82:85]
	buffer_load_dwordx4 v[38:41], v1, s[4:7], s23 offen sc0 nt
	s_or_b32 s23, s22, 0x18000
	s_or_b32 s22, s22, 0x1c000
	v_mfma_f32_16x16x32_bf16 v[62:65], v[202:205], v[226:229], v[62:65]
	s_waitcnt lgkmcnt(5)
	v_mfma_f32_16x16x32_bf16 v[94:97], v[178:181], v[230:233], v[94:97]
	v_mfma_f32_16x16x32_bf16 v[86:89], v[194:197], v[230:233], v[86:89]
	v_mfma_f32_16x16x32_bf16 v[70:73], v[198:201], v[230:233], v[70:73]
	buffer_load_dwordx4 v[42:45], v1, s[4:7], s23 offen sc0 nt
	v_mfma_f32_16x16x32_bf16 v[54:57], v[202:205], v[230:233], v[54:57]
	s_waitcnt lgkmcnt(4)
	v_mfma_f32_16x16x32_bf16 v[78:81], v[178:181], v[234:237], v[78:81]
	v_mfma_f32_16x16x32_bf16 v[66:69], v[194:197], v[234:237], v[66:69]
	v_mfma_f32_16x16x32_bf16 v[58:61], v[198:201], v[234:237], v[58:61]
	buffer_load_dwordx4 v[46:49], v1, s[4:7], s22 offen sc0 nt
	v_mfma_f32_16x16x32_bf16 v[50:53], v[202:205], v[234:237], v[50:53]
	s_setprio 0
	s_waitcnt lgkmcnt(0)
	s_barrier
	ds_read_b128 v[178:181], v182 offset:33792
	ds_read_b128 v[194:197], v182 offset:35840
	ds_read_b128 v[198:201], v182 offset:37888
	ds_read_b128 v[202:205], v182 offset:39936
	ds_read_b128 v[206:209], v238 offset:1024
	ds_read_b128 v[210:213], v238 offset:3072
	ds_read_b128 v[214:217], v238 offset:5120
	ds_read_b128 v[218:221], v238 offset:7168
	ds_read_b128 v[222:225], v238 offset:9216
	ds_read_b128 v[226:229], v238 offset:11264
	ds_read_b128 v[230:233], v238 offset:13312
	ds_read_b128 v[234:237], v238 offset:15360
	v_add_u32_e32 v182, s19, v190
	s_waitcnt vmcnt(11)
	ds_write_b128 v182, v[2:5] offset:32768
	s_waitcnt vmcnt(10)
	ds_write_b128 v182, v[6:9] offset:40960
	s_waitcnt vmcnt(9)
	ds_write_b128 v182, v[14:17] offset:49152
	s_waitcnt vmcnt(8)
	ds_write_b128 v182, v[26:29] offset:57344
	s_waitcnt lgkmcnt(0)
	s_barrier
	s_setprio 1
	s_lshl_b32 s21, s21, 7
	s_and_b32 s21, s21, 0x780
	s_or_b32 s21, s21, s14
	s_or_b32 s22, s21, 0x20000
	s_waitcnt lgkmcnt(11)
	v_mfma_f32_16x16x32_bf16 v[174:177], v[178:181], v[206:209], v[174:177]
	v_mfma_f32_16x16x32_bf16 v[170:173], v[194:197], v[206:209], v[170:173]
	v_mfma_f32_16x16x32_bf16 v[158:161], v[198:201], v[206:209], v[158:161]
	v_mfma_f32_16x16x32_bf16 v[142:145], v[202:205], v[206:209], v[142:145]
	s_waitcnt lgkmcnt(10)
	v_mfma_f32_16x16x32_bf16 v[166:169], v[178:181], v[210:213], v[166:169]
	v_mfma_f32_16x16x32_bf16 v[162:165], v[194:197], v[210:213], v[162:165]
	buffer_load_dwordx4 v[2:5], v188, s[0:3], s21 offen sc1
	v_mfma_f32_16x16x32_bf16 v[146:149], v[198:201], v[210:213], v[146:149]
	v_mfma_f32_16x16x32_bf16 v[122:125], v[202:205], v[210:213], v[122:125]
	s_waitcnt lgkmcnt(9)
	v_mfma_f32_16x16x32_bf16 v[154:157], v[178:181], v[214:217], v[154:157]
	v_mfma_f32_16x16x32_bf16 v[150:153], v[194:197], v[214:217], v[150:153]
	v_mfma_f32_16x16x32_bf16 v[130:133], v[198:201], v[214:217], v[130:133]
	v_mfma_f32_16x16x32_bf16 v[106:109], v[202:205], v[214:217], v[106:109]
	s_waitcnt lgkmcnt(8)
	v_mfma_f32_16x16x32_bf16 v[138:141], v[178:181], v[218:221], v[138:141]
	v_mfma_f32_16x16x32_bf16 v[134:137], v[194:197], v[218:221], v[134:137]
	buffer_load_dwordx4 v[6:9], v188, s[0:3], s22 offen sc1
	s_or_b32 s22, s21, 0x40000
	s_or_b32 s21, s21, 0x60000
	v_mfma_f32_16x16x32_bf16 v[114:117], v[198:201], v[218:221], v[114:117]
	v_mfma_f32_16x16x32_bf16 v[90:93], v[202:205], v[218:221], v[90:93]
	s_waitcnt lgkmcnt(7)
	v_mfma_f32_16x16x32_bf16 v[126:129], v[178:181], v[222:225], v[126:129]
	v_mfma_f32_16x16x32_bf16 v[118:121], v[194:197], v[222:225], v[118:121]
	v_mfma_f32_16x16x32_bf16 v[98:101], v[198:201], v[222:225], v[98:101]
	v_mfma_f32_16x16x32_bf16 v[74:77], v[202:205], v[222:225], v[74:77]
	s_waitcnt lgkmcnt(6)
	v_mfma_f32_16x16x32_bf16 v[110:113], v[178:181], v[226:229], v[110:113]
	v_mfma_f32_16x16x32_bf16 v[102:105], v[194:197], v[226:229], v[102:105]
	buffer_load_dwordx4 v[14:17], v188, s[0:3], s22 offen sc1
	v_mfma_f32_16x16x32_bf16 v[82:85], v[198:201], v[226:229], v[82:85]
	v_mfma_f32_16x16x32_bf16 v[62:65], v[202:205], v[226:229], v[62:65]
	s_waitcnt lgkmcnt(5)
	v_mfma_f32_16x16x32_bf16 v[94:97], v[178:181], v[230:233], v[94:97]
	v_mfma_f32_16x16x32_bf16 v[86:89], v[194:197], v[230:233], v[86:89]
	v_mfma_f32_16x16x32_bf16 v[70:73], v[198:201], v[230:233], v[70:73]
	v_mfma_f32_16x16x32_bf16 v[54:57], v[202:205], v[230:233], v[54:57]
	s_waitcnt lgkmcnt(4)
	v_mfma_f32_16x16x32_bf16 v[78:81], v[178:181], v[234:237], v[78:81]
	v_mfma_f32_16x16x32_bf16 v[66:69], v[194:197], v[234:237], v[66:69]
	buffer_load_dwordx4 v[26:29], v188, s[0:3], s21 offen sc1
	v_mfma_f32_16x16x32_bf16 v[58:61], v[198:201], v[234:237], v[58:61]
	v_mfma_f32_16x16x32_bf16 v[50:53], v[202:205], v[234:237], v[50:53]
	s_setprio 0
	s_and_b32 s21, s20, 15
	s_cmp_lg_u32 s21, 15
	s_cbranch_scc1 .LBB1_3
	s_and_b32 s21, s18, 32
	s_add_i32 s21, s21, s12
	s_lshl_b32 s21, s21, 6
	s_and_b32 s21, s21, 0x3f00
	v_add_lshl_u32 v182, v193, s21, 9
	v_lshl_add_u64 v[206:207], v[184:185], 0, v[182:183]
	v_add_co_u32_e32 v208, vcc, s8, v206
	v_pk_add_f32 v[176:177], v[242:243], v[176:177]
	v_addc_co_u32_e32 v209, vcc, 0, v207, vcc
	v_add_co_u32_e32 v210, vcc, s15, v206
	v_pk_add_f32 v[174:175], v[240:241], v[174:175]
	s_nop 0
	v_addc_co_u32_e32 v211, vcc, 0, v207, vcc
	v_add_co_u32_e32 v212, vcc, s9, v206
	v_pk_add_f32 v[68:69], v[246:247], v[68:69]
	v_addc_co_u32_e32 v213, vcc, 0, v207, vcc
	v_add_co_u32_e32 v214, vcc, s16, v206
	v_pk_add_f32 v[66:67], v[244:245], v[66:67]
	s_nop 0
	v_addc_co_u32_e32 v215, vcc, 0, v207, vcc
	v_add_co_u32_e32 v216, vcc, s10, v206
	v_pk_add_f32 v[168:169], v[242:243], v[168:169]
	s_nop 0
	v_addc_co_u32_e32 v217, vcc, 0, v207, vcc
	v_add_co_u32_e32 v218, vcc, s17, v206
	v_pk_add_f32 v[166:167], v[240:241], v[166:167]
	s_nop 0
	v_addc_co_u32_e32 v219, vcc, 0, v207, vcc
	v_add_co_u32_e32 v220, vcc, s11, v206
	v_pk_add_f32 v[156:157], v[242:243], v[156:157]
	s_nop 0
	v_addc_co_u32_e32 v221, vcc, 0, v207, vcc
	v_pk_add_f32 v[154:155], v[240:241], v[154:155]
	v_pk_add_f32 v[140:141], v[242:243], v[140:141]
	v_pk_add_f32 v[138:139], v[240:241], v[138:139]
	v_pk_add_f32 v[128:129], v[242:243], v[128:129]
	v_pk_add_f32 v[126:127], v[240:241], v[126:127]
	v_pk_add_f32 v[112:113], v[242:243], v[112:113]
	v_pk_add_f32 v[110:111], v[240:241], v[110:111]
	v_pk_add_f32 v[96:97], v[242:243], v[96:97]
	v_pk_add_f32 v[94:95], v[240:241], v[94:95]
	v_pk_add_f32 v[80:81], v[242:243], v[80:81]
	v_pk_add_f32 v[78:79], v[240:241], v[78:79]
	v_pk_add_f32 v[172:173], v[246:247], v[172:173]
	v_pk_add_f32 v[170:171], v[244:245], v[170:171]
	v_pk_add_f32 v[164:165], v[246:247], v[164:165]
	v_pk_add_f32 v[162:163], v[244:245], v[162:163]
	v_pk_add_f32 v[152:153], v[246:247], v[152:153]
	v_pk_add_f32 v[150:151], v[244:245], v[150:151]
	v_pk_add_f32 v[136:137], v[246:247], v[136:137]
	v_pk_add_f32 v[134:135], v[244:245], v[134:135]
	v_pk_add_f32 v[120:121], v[246:247], v[120:121]
	v_pk_add_f32 v[118:119], v[244:245], v[118:119]
	v_pk_add_f32 v[104:105], v[246:247], v[104:105]
	v_pk_add_f32 v[102:103], v[244:245], v[102:103]
	v_pk_add_f32 v[88:89], v[246:247], v[88:89]
	v_pk_add_f32 v[86:87], v[244:245], v[86:87]
	global_store_dwordx4 v[206:207], v[174:177], off
	global_store_dwordx4 v[208:209], v[166:169], off
	global_store_dwordx4 v[210:211], v[154:157], off
	global_store_dwordx4 v[212:213], v[138:141], off
	global_store_dwordx4 v[214:215], v[126:129], off
	global_store_dwordx4 v[216:217], v[110:113], off
	global_store_dwordx4 v[218:219], v[94:97], off
	global_store_dwordx4 v[220:221], v[78:81], off
	global_store_dwordx4 v[206:207], v[170:173], off offset:64
	global_store_dwordx4 v[208:209], v[162:165], off offset:64
	global_store_dwordx4 v[210:211], v[150:153], off offset:64
	global_store_dwordx4 v[212:213], v[134:137], off offset:64
	global_store_dwordx4 v[214:215], v[118:121], off offset:64
	global_store_dwordx4 v[216:217], v[102:105], off offset:64
	global_store_dwordx4 v[218:219], v[86:89], off offset:64
	global_store_dwordx4 v[220:221], v[66:69], off offset:64
	v_pk_add_f32 v[60:61], v[250:251], v[60:61]
	v_pk_add_f32 v[58:59], v[248:249], v[58:59]
	v_pk_add_f32 v[68:69], v[250:251], v[160:161]
	v_pk_add_f32 v[66:67], v[248:249], v[158:159]
	global_store_dwordx4 v[206:207], v[66:69], off offset:128
	global_store_dwordx4 v[220:221], v[58:61], off offset:128
	v_pk_add_f32 v[52:53], v[254:255], v[52:53]
	v_pk_add_f32 v[68:69], v[250:251], v[148:149]
	v_pk_add_f32 v[66:67], v[248:249], v[146:147]
	v_pk_add_f32 v[60:61], v[254:255], v[144:145]
	v_pk_add_f32 v[58:59], v[252:253], v[142:143]
	global_store_dwordx4 v[208:209], v[66:69], off offset:128
	global_store_dwordx4 v[206:207], v[58:61], off offset:192
	v_pk_add_f32 v[50:51], v[252:253], v[50:51]
	v_pk_add_f32 v[68:69], v[250:251], v[132:133]
	v_pk_add_f32 v[66:67], v[248:249], v[130:131]
	v_pk_add_f32 v[60:61], v[254:255], v[124:125]
	v_pk_add_f32 v[58:59], v[252:253], v[122:123]
	global_store_dwordx4 v[210:211], v[66:69], off offset:128
	global_store_dwordx4 v[208:209], v[58:61], off offset:192
	v_pk_add_f32 v[56:57], v[254:255], v[56:57]
	v_pk_add_f32 v[68:69], v[250:251], v[116:117]
	v_pk_add_f32 v[66:67], v[248:249], v[114:115]
	v_pk_add_f32 v[60:61], v[254:255], v[108:109]
	v_pk_add_f32 v[58:59], v[252:253], v[106:107]
	global_store_dwordx4 v[212:213], v[66:69], off offset:128
	global_store_dwordx4 v[210:211], v[58:61], off offset:192
	v_pk_add_f32 v[54:55], v[252:253], v[54:55]
	v_pk_add_f32 v[68:69], v[250:251], v[100:101]
	v_pk_add_f32 v[66:67], v[248:249], v[98:99]
	v_pk_add_f32 v[60:61], v[254:255], v[92:93]
	v_pk_add_f32 v[58:59], v[252:253], v[90:91]
	global_store_dwordx4 v[214:215], v[66:69], off offset:128
	global_store_dwordx4 v[212:213], v[58:61], off offset:192
	global_store_dwordx4 v[220:221], v[50:53], off offset:192
	v_pk_add_f32 v[68:69], v[250:251], v[84:85]
	v_pk_add_f32 v[66:67], v[248:249], v[82:83]
	v_pk_add_f32 v[60:61], v[254:255], v[76:77]
	v_pk_add_f32 v[58:59], v[252:253], v[74:75]
	global_store_dwordx4 v[216:217], v[66:69], off offset:128
	global_store_dwordx4 v[214:215], v[58:61], off offset:192
	v_mov_b32_e32 v50, 0
	v_pk_add_f32 v[68:69], v[250:251], v[72:73]
	v_pk_add_f32 v[66:67], v[248:249], v[70:71]
	v_pk_add_f32 v[60:61], v[254:255], v[64:65]
	v_pk_add_f32 v[58:59], v[252:253], v[62:63]
	global_store_dwordx4 v[218:219], v[66:69], off offset:128
	global_store_dwordx4 v[216:217], v[58:61], off offset:192
	global_store_dwordx4 v[218:219], v[54:57], off offset:192
	v_mov_b32_e32 v51, v50
	v_mov_b32_e32 v52, v50
	v_mov_b32_e32 v53, v50
	v_mov_b32_e32 v58, v50
	v_mov_b32_e32 v59, v50
	v_mov_b32_e32 v60, v50
	v_mov_b32_e32 v61, v50
	v_mov_b32_e32 v66, v50
	v_mov_b32_e32 v67, v50
	v_mov_b32_e32 v68, v50
	v_mov_b32_e32 v69, v50
	v_mov_b32_e32 v78, v50
	v_mov_b32_e32 v79, v50
	v_mov_b32_e32 v80, v50
	v_mov_b32_e32 v81, v50
	v_mov_b32_e32 v54, v50
	v_mov_b32_e32 v55, v50
	v_mov_b32_e32 v56, v50
	v_mov_b32_e32 v57, v50
	v_mov_b32_e32 v70, v50
	v_mov_b32_e32 v71, v50
	v_mov_b32_e32 v72, v50
	v_mov_b32_e32 v73, v50
	v_mov_b32_e32 v86, v50
	v_mov_b32_e32 v87, v50
	v_mov_b32_e32 v88, v50
	v_mov_b32_e32 v89, v50
	v_mov_b32_e32 v94, v50
	v_mov_b32_e32 v95, v50
	v_mov_b32_e32 v96, v50
	v_mov_b32_e32 v97, v50
	v_mov_b32_e32 v62, v50
	v_mov_b32_e32 v63, v50
	v_mov_b32_e32 v64, v50
	v_mov_b32_e32 v65, v50
	v_mov_b32_e32 v82, v50
	v_mov_b32_e32 v83, v50
	v_mov_b32_e32 v84, v50
	v_mov_b32_e32 v85, v50
	v_mov_b32_e32 v102, v50
	v_mov_b32_e32 v103, v50
	v_mov_b32_e32 v104, v50
	v_mov_b32_e32 v105, v50
	v_mov_b32_e32 v110, v50
	v_mov_b32_e32 v111, v50
	v_mov_b32_e32 v112, v50
	v_mov_b32_e32 v113, v50
	v_mov_b32_e32 v74, v50
	v_mov_b32_e32 v75, v50
	v_mov_b32_e32 v76, v50
	v_mov_b32_e32 v77, v50
	v_mov_b32_e32 v98, v50
	v_mov_b32_e32 v99, v50
	v_mov_b32_e32 v100, v50
	v_mov_b32_e32 v101, v50
	v_mov_b32_e32 v118, v50
	v_mov_b32_e32 v119, v50
	v_mov_b32_e32 v120, v50
	v_mov_b32_e32 v121, v50
	v_mov_b32_e32 v126, v50
	v_mov_b32_e32 v127, v50
	v_mov_b32_e32 v128, v50
	v_mov_b32_e32 v129, v50
	v_mov_b32_e32 v90, v50
	v_mov_b32_e32 v91, v50
	v_mov_b32_e32 v92, v50
	v_mov_b32_e32 v93, v50
	v_mov_b32_e32 v114, v50
	v_mov_b32_e32 v115, v50
	v_mov_b32_e32 v116, v50
	v_mov_b32_e32 v117, v50
	v_mov_b32_e32 v134, v50
	v_mov_b32_e32 v135, v50
	v_mov_b32_e32 v136, v50
	v_mov_b32_e32 v137, v50
	v_mov_b32_e32 v138, v50
	v_mov_b32_e32 v139, v50
	v_mov_b32_e32 v140, v50
	v_mov_b32_e32 v141, v50
	v_mov_b32_e32 v106, v50
	v_mov_b32_e32 v107, v50
	v_mov_b32_e32 v108, v50
	v_mov_b32_e32 v109, v50
	v_mov_b32_e32 v130, v50
	v_mov_b32_e32 v131, v50
	v_mov_b32_e32 v132, v50
	v_mov_b32_e32 v133, v50
	v_mov_b32_e32 v150, v50
	v_mov_b32_e32 v151, v50
	v_mov_b32_e32 v152, v50
	v_mov_b32_e32 v153, v50
	v_mov_b32_e32 v154, v50
	v_mov_b32_e32 v155, v50
	v_mov_b32_e32 v156, v50
	v_mov_b32_e32 v157, v50
	v_mov_b32_e32 v122, v50
	v_mov_b32_e32 v123, v50
	v_mov_b32_e32 v124, v50
	v_mov_b32_e32 v125, v50
	v_mov_b32_e32 v146, v50
	v_mov_b32_e32 v147, v50
	v_mov_b32_e32 v148, v50
	v_mov_b32_e32 v149, v50
	v_mov_b32_e32 v162, v50
	v_mov_b32_e32 v163, v50
	v_mov_b32_e32 v164, v50
	v_mov_b32_e32 v165, v50
	v_mov_b32_e32 v166, v50
	v_mov_b32_e32 v167, v50
	v_mov_b32_e32 v168, v50
	v_mov_b32_e32 v169, v50
	v_mov_b32_e32 v142, v50
	v_mov_b32_e32 v143, v50
	v_mov_b32_e32 v144, v50
	v_mov_b32_e32 v145, v50
	v_mov_b32_e32 v158, v50
	v_mov_b32_e32 v159, v50
	v_mov_b32_e32 v160, v50
	v_mov_b32_e32 v161, v50
	v_mov_b32_e32 v170, v50
	v_mov_b32_e32 v171, v50
	v_mov_b32_e32 v172, v50
	v_mov_b32_e32 v173, v50
	v_mov_b32_e32 v174, v50
	v_mov_b32_e32 v175, v50
	v_mov_b32_e32 v176, v50
	v_mov_b32_e32 v177, v50
	s_cmp_eq_u32 s20, 15
	s_cbranch_scc1 .Lpd_tail
	s_branch .LBB1_3
.Lpd_tail:
	s_waitcnt lgkmcnt(0)
	s_barrier
	s_add_i32 s20, s20, 1
	s_add_i32 s18, s18, 2
	v_add_u32_e32 v182, s19, v191
	v_add_u32_e32 v238, s19, v192
	ds_read_b128 v[178:181], v182 offset:32768
	ds_read_b128 v[194:197], v182 offset:34816
	ds_read_b128 v[198:201], v182 offset:36864
	ds_read_b128 v[202:205], v182 offset:38912
	ds_read_b128 v[206:209], v238
	ds_read_b128 v[210:213], v238 offset:2048
	ds_read_b128 v[214:217], v238 offset:4096
	ds_read_b128 v[218:221], v238 offset:6144
	ds_read_b128 v[222:225], v238 offset:8192
	ds_read_b128 v[226:229], v238 offset:10240
	ds_read_b128 v[230:233], v238 offset:12288
	ds_read_b128 v[234:237], v238 offset:14336
	s_min_u32 s21, s20, 29
	s_xor_b32 s19, s19, 0x10000
	v_add_u32_e32 v239, s19, v189
	s_waitcnt vmcnt(43)
	v_cvt_pk_bf16_f32 v13, v12, v13
	v_cvt_pk_bf16_f32 v12, v10, v11
	s_waitcnt vmcnt(42)
	v_cvt_pk_bf16_f32 v11, v20, v21
	v_cvt_pk_bf16_f32 v10, v18, v19
	ds_write2st64_b64 v239, v[12:13], v[10:11] offset1:8
	s_waitcnt vmcnt(41)
	v_cvt_pk_bf16_f32 v11, v24, v25
	v_cvt_pk_bf16_f32 v10, v22, v23
	s_waitcnt vmcnt(40)
	v_cvt_pk_bf16_f32 v13, v32, v33
	v_cvt_pk_bf16_f32 v12, v30, v31
	ds_write2st64_b64 v239, v[10:11], v[12:13] offset0:16 offset1:24
	s_waitcnt vmcnt(39)
	v_cvt_pk_bf16_f32 v11, v36, v37
	v_cvt_pk_bf16_f32 v10, v34, v35
	s_waitcnt vmcnt(38)
	v_cvt_pk_bf16_f32 v13, v40, v41
	v_cvt_pk_bf16_f32 v12, v38, v39
	ds_write2st64_b64 v239, v[10:11], v[12:13] offset0:32 offset1:40
	s_waitcnt vmcnt(37)
	v_cvt_pk_bf16_f32 v11, v44, v45
	v_cvt_pk_bf16_f32 v10, v42, v43
	s_waitcnt vmcnt(36)
	v_cvt_pk_bf16_f32 v13, v48, v49
	v_cvt_pk_bf16_f32 v12, v46, v47
	ds_write2st64_b64 v239, v[10:11], v[12:13] offset0:48 offset1:56
	s_waitcnt lgkmcnt(0)
	s_add_i32 s21, s21, 2
	s_barrier
	s_setprio 1
	s_lshl_b32 s22, s21, 1
	s_and_b32 s22, s22, 0x60
	s_add_i32 s22, s22, s12
	s_lshl_b32 s22, s22, 6
	s_and_b32 s22, s22, 0x3f00
	s_or_b32 s22, s22, s13
	s_lshl_b32 s23, s21, 23
	s_lshl_b32 s22, s22, 9
	s_and_b32 s23, s23, 0x7000000
	s_or_b32 s22, s22, s23
	s_lshl_b32 s23, s21, 8
	s_and_b32 s23, s23, 0x100
	s_or_b32 s22, s22, s23
	s_or_b32 s23, s22, 0x4000
	s_waitcnt lgkmcnt(11)
	v_mfma_f32_16x16x32_bf16 v[174:177], v[178:181], v[206:209], v[174:177]
	v_mfma_f32_16x16x32_bf16 v[170:173], v[194:197], v[206:209], v[170:173]
	v_mfma_f32_16x16x32_bf16 v[158:161], v[198:201], v[206:209], v[158:161]
	buffer_load_dwordx4 v[10:13], v1, s[4:7], s22 offen sc0 nt
	v_mfma_f32_16x16x32_bf16 v[142:145], v[202:205], v[206:209], v[142:145]
	s_waitcnt lgkmcnt(10)
	v_mfma_f32_16x16x32_bf16 v[166:169], v[178:181], v[210:213], v[166:169]
	v_mfma_f32_16x16x32_bf16 v[162:165], v[194:197], v[210:213], v[162:165]
	v_mfma_f32_16x16x32_bf16 v[146:149], v[198:201], v[210:213], v[146:149]
	buffer_load_dwordx4 v[18:21], v1, s[4:7], s23 offen sc0 nt
	s_or_b32 s23, s22, 0x8000
	v_mfma_f32_16x16x32_bf16 v[122:125], v[202:205], v[210:213], v[122:125]
	s_waitcnt lgkmcnt(9)
	v_mfma_f32_16x16x32_bf16 v[154:157], v[178:181], v[214:217], v[154:157]
	v_mfma_f32_16x16x32_bf16 v[150:153], v[194:197], v[214:217], v[150:153]
	v_mfma_f32_16x16x32_bf16 v[130:133], v[198:201], v[214:217], v[130:133]
	buffer_load_dwordx4 v[22:25], v1, s[4:7], s23 offen sc0 nt
	s_or_b32 s23, s22, 0xc000
	v_mfma_f32_16x16x32_bf16 v[106:109], v[202:205], v[214:217], v[106:109]
	s_waitcnt lgkmcnt(8)
	v_mfma_f32_16x16x32_bf16 v[138:141], v[178:181], v[218:221], v[138:141]
	v_mfma_f32_16x16x32_bf16 v[134:137], v[194:197], v[218:221], v[134:137]
	v_mfma_f32_16x16x32_bf16 v[114:117], v[198:201], v[218:221], v[114:117]
	buffer_load_dwordx4 v[30:33], v1, s[4:7], s23 offen sc0 nt
	s_or_b32 s23, s22, 0x10000
	v_mfma_f32_16x16x32_bf16 v[90:93], v[202:205], v[218:221], v[90:93]
	s_waitcnt lgkmcnt(7)
	v_mfma_f32_16x16x32_bf16 v[126:129], v[178:181], v[222:225], v[126:129]
	v_mfma_f32_16x16x32_bf16 v[118:121], v[194:197], v[222:225], v[118:121]
	v_mfma_f32_16x16x32_bf16 v[98:101], v[198:201], v[222:225], v[98:101]
	buffer_load_dwordx4 v[34:37], v1, s[4:7], s23 offen sc0 nt
	s_or_b32 s23, s22, 0x14000
	v_mfma_f32_16x16x32_bf16 v[74:77], v[202:205], v[222:225], v[74:77]
	s_waitcnt lgkmcnt(6)
	v_mfma_f32_16x16x32_bf16 v[110:113], v[178:181], v[226:229], v[110:113]
	v_mfma_f32_16x16x32_bf16 v[102:105], v[194:197], v[226:229], v[102:105]
	v_mfma_f32_16x16x32_bf16 v[82:85], v[198:201], v[226:229], v[82:85]
	buffer_load_dwordx4 v[38:41], v1, s[4:7], s23 offen sc0 nt
	s_or_b32 s23, s22, 0x18000
	s_or_b32 s22, s22, 0x1c000
	v_mfma_f32_16x16x32_bf16 v[62:65], v[202:205], v[226:229], v[62:65]
	s_waitcnt lgkmcnt(5)
	v_mfma_f32_16x16x32_bf16 v[94:97], v[178:181], v[230:233], v[94:97]
	v_mfma_f32_16x16x32_bf16 v[86:89], v[194:197], v[230:233], v[86:89]
	v_mfma_f32_16x16x32_bf16 v[70:73], v[198:201], v[230:233], v[70:73]
	buffer_load_dwordx4 v[42:45], v1, s[4:7], s23 offen sc0 nt
	v_mfma_f32_16x16x32_bf16 v[54:57], v[202:205], v[230:233], v[54:57]
	s_waitcnt lgkmcnt(4)
	v_mfma_f32_16x16x32_bf16 v[78:81], v[178:181], v[234:237], v[78:81]
	v_mfma_f32_16x16x32_bf16 v[66:69], v[194:197], v[234:237], v[66:69]
	v_mfma_f32_16x16x32_bf16 v[58:61], v[198:201], v[234:237], v[58:61]
	buffer_load_dwordx4 v[46:49], v1, s[4:7], s22 offen sc0 nt
	v_mfma_f32_16x16x32_bf16 v[50:53], v[202:205], v[234:237], v[50:53]
	s_setprio 0
	s_waitcnt lgkmcnt(0)
	s_barrier
	ds_read_b128 v[178:181], v182 offset:33792
	ds_read_b128 v[194:197], v182 offset:35840
	ds_read_b128 v[198:201], v182 offset:37888
	ds_read_b128 v[202:205], v182 offset:39936
	ds_read_b128 v[206:209], v238 offset:1024
	ds_read_b128 v[210:213], v238 offset:3072
	ds_read_b128 v[214:217], v238 offset:5120
	ds_read_b128 v[218:221], v238 offset:7168
	ds_read_b128 v[222:225], v238 offset:9216
	ds_read_b128 v[226:229], v238 offset:11264
	ds_read_b128 v[230:233], v238 offset:13312
	ds_read_b128 v[234:237], v238 offset:15360
	v_add_u32_e32 v182, s19, v190
	s_waitcnt vmcnt(43)
	ds_write_b128 v182, v[2:5] offset:32768
	s_waitcnt vmcnt(42)
	ds_write_b128 v182, v[6:9] offset:40960
	s_waitcnt vmcnt(41)
	ds_write_b128 v182, v[14:17] offset:49152
	s_waitcnt vmcnt(40)
	ds_write_b128 v182, v[26:29] offset:57344
	s_waitcnt lgkmcnt(0)
	s_barrier
	s_setprio 1
	s_lshl_b32 s21, s21, 7
	s_and_b32 s21, s21, 0x780
	s_or_b32 s21, s21, s14
	s_or_b32 s22, s21, 0x20000
	s_waitcnt lgkmcnt(11)
	v_mfma_f32_16x16x32_bf16 v[174:177], v[178:181], v[206:209], v[174:177]
	v_mfma_f32_16x16x32_bf16 v[170:173], v[194:197], v[206:209], v[170:173]
	v_mfma_f32_16x16x32_bf16 v[158:161], v[198:201], v[206:209], v[158:161]
	v_mfma_f32_16x16x32_bf16 v[142:145], v[202:205], v[206:209], v[142:145]
	s_waitcnt lgkmcnt(10)
	v_mfma_f32_16x16x32_bf16 v[166:169], v[178:181], v[210:213], v[166:169]
	v_mfma_f32_16x16x32_bf16 v[162:165], v[194:197], v[210:213], v[162:165]
	buffer_load_dwordx4 v[2:5], v188, s[0:3], s21 offen sc1
	v_mfma_f32_16x16x32_bf16 v[146:149], v[198:201], v[210:213], v[146:149]
	v_mfma_f32_16x16x32_bf16 v[122:125], v[202:205], v[210:213], v[122:125]
	s_waitcnt lgkmcnt(9)
	v_mfma_f32_16x16x32_bf16 v[154:157], v[178:181], v[214:217], v[154:157]
	v_mfma_f32_16x16x32_bf16 v[150:153], v[194:197], v[214:217], v[150:153]
	v_mfma_f32_16x16x32_bf16 v[130:133], v[198:201], v[214:217], v[130:133]
	v_mfma_f32_16x16x32_bf16 v[106:109], v[202:205], v[214:217], v[106:109]
	s_waitcnt lgkmcnt(8)
	v_mfma_f32_16x16x32_bf16 v[138:141], v[178:181], v[218:221], v[138:141]
	v_mfma_f32_16x16x32_bf16 v[134:137], v[194:197], v[218:221], v[134:137]
	buffer_load_dwordx4 v[6:9], v188, s[0:3], s22 offen sc1
	s_or_b32 s22, s21, 0x40000
	s_or_b32 s21, s21, 0x60000
	v_mfma_f32_16x16x32_bf16 v[114:117], v[198:201], v[218:221], v[114:117]
	v_mfma_f32_16x16x32_bf16 v[90:93], v[202:205], v[218:221], v[90:93]
	s_waitcnt lgkmcnt(7)
	v_mfma_f32_16x16x32_bf16 v[126:129], v[178:181], v[222:225], v[126:129]
	v_mfma_f32_16x16x32_bf16 v[118:121], v[194:197], v[222:225], v[118:121]
	v_mfma_f32_16x16x32_bf16 v[98:101], v[198:201], v[222:225], v[98:101]
	v_mfma_f32_16x16x32_bf16 v[74:77], v[202:205], v[222:225], v[74:77]
	s_waitcnt lgkmcnt(6)
	v_mfma_f32_16x16x32_bf16 v[110:113], v[178:181], v[226:229], v[110:113]
	v_mfma_f32_16x16x32_bf16 v[102:105], v[194:197], v[226:229], v[102:105]
	buffer_load_dwordx4 v[14:17], v188, s[0:3], s22 offen sc1
	v_mfma_f32_16x16x32_bf16 v[82:85], v[198:201], v[226:229], v[82:85]
	v_mfma_f32_16x16x32_bf16 v[62:65], v[202:205], v[226:229], v[62:65]
	s_waitcnt lgkmcnt(5)
	v_mfma_f32_16x16x32_bf16 v[94:97], v[178:181], v[230:233], v[94:97]
	v_mfma_f32_16x16x32_bf16 v[86:89], v[194:197], v[230:233], v[86:89]
	v_mfma_f32_16x16x32_bf16 v[70:73], v[198:201], v[230:233], v[70:73]
	v_mfma_f32_16x16x32_bf16 v[54:57], v[202:205], v[230:233], v[54:57]
	s_waitcnt lgkmcnt(4)
	v_mfma_f32_16x16x32_bf16 v[78:81], v[178:181], v[234:237], v[78:81]
	v_mfma_f32_16x16x32_bf16 v[66:69], v[194:197], v[234:237], v[66:69]
	buffer_load_dwordx4 v[26:29], v188, s[0:3], s21 offen sc1
	v_mfma_f32_16x16x32_bf16 v[58:61], v[198:201], v[234:237], v[58:61]
	v_mfma_f32_16x16x32_bf16 v[50:53], v[202:205], v[234:237], v[50:53]
	s_setprio 0
	s_branch .LBB1_3

	.amdhsa_kernel _Z11gemm_kernelPKfPKDF16bS0_Pf
		.amdhsa_group_segment_fixed_size 131072
		.amdhsa_private_segment_fixed_size 0
		.amdhsa_kernarg_size 32
		.amdhsa_user_sgpr_count 2
		.amdhsa_user_sgpr_dispatch_ptr 0
		.amdhsa_user_sgpr_queue_ptr 0
		.amdhsa_user_sgpr_kernarg_segment_ptr 1
		.amdhsa_user_sgpr_dispatch_id 0
		.amdhsa_user_sgpr_kernarg_preload_length 0
		.amdhsa_user_sgpr_kernarg_preload_offset 0
		.amdhsa_user_sgpr_private_segment_size 0
		.amdhsa_uses_dynamic_stack 0
		.amdhsa_enable_private_segment 0
		.amdhsa_system_sgpr_workgroup_id_x 1
		.amdhsa_system_sgpr_workgroup_id_y 0
		.amdhsa_system_sgpr_workgroup_id_z 0
		.amdhsa_system_sgpr_workgroup_info 0
		.amdhsa_system_vgpr_workitem_id 0
		.amdhsa_next_free_vgpr 256
		.amdhsa_next_free_sgpr 96
		.amdhsa_accum_offset 256
		.amdhsa_reserve_vcc 1
		.amdhsa_float_round_mode_32 0
		.amdhsa_float_round_mode_16_64 0
		.amdhsa_float_denorm_mode_32 3
		.amdhsa_float_denorm_mode_16_64 3
		.amdhsa_dx10_clamp 1
		.amdhsa_ieee_mode 1
		.amdhsa_fp16_overflow 0
		.amdhsa_tg_split 0
		.amdhsa_exception_fp_ieee_invalid_op 0
		.amdhsa_exception_fp_denorm_src 0
		.amdhsa_exception_fp_ieee_div_zero 0
		.amdhsa_exception_fp_ieee_overflow 0
		.amdhsa_exception_fp_ieee_underflow 0
		.amdhsa_exception_fp_ieee_inexact 0
		.amdhsa_exception_int_div_zero 0
	.end_amdhsa_kernel

amdhsa.kernels:
  - .agpr_count:     0
    .args:
      - .actual_access:  read_only
        .address_space:  global
        .offset:         0
        .size:           8
        .value_kind:     global_buffer
      - .actual_access:  read_only
        .address_space:  global
        .offset:         8
        .size:           8
        .value_kind:     global_buffer
      - .actual_access:  write_only
        .address_space:  global
        .offset:         16
        .size:           8
        .value_kind:     global_buffer
      - .actual_access:  write_only
        .address_space:  global
        .offset:         24
        .size:           8
        .value_kind:     global_buffer
    .group_segment_fixed_size: 0
    .kernarg_segment_align: 8
    .kernarg_segment_size: 32
    .language:       OpenCL C
    .language_version:
      - 2
      - 0
    .max_flat_workgroup_size: 256
    .name:           _Z11prep_kernelPKfS0_PDF16bPf
    .private_segment_fixed_size: 0
    .sgpr_count:     12
    .sgpr_spill_count: 0
    .symbol:         _Z11prep_kernelPKfS0_PDF16bPf.kd
    .uniform_work_group_size: 1
    .uses_dynamic_stack: false
    .vgpr_count:     16
    .vgpr_spill_count: 0
    .wavefront_size: 64
  - .agpr_count:     0
    .args:
      - .actual_access:  read_only
        .address_space:  global
        .offset:         0
        .size:           8
        .value_kind:     global_buffer
      - .actual_access:  read_only
        .address_space:  global
        .offset:         8
        .size:           8
        .value_kind:     global_buffer
      - .actual_access:  read_only
        .address_space:  global
        .offset:         16
        .size:           8
        .value_kind:     global_buffer
      - .actual_access:  write_only
        .address_space:  global
        .offset:         24
        .size:           8
        .value_kind:     global_buffer
    .group_segment_fixed_size: 131072
    .kernarg_segment_align: 8
    .kernarg_segment_size: 32
    .language:       OpenCL C
    .language_version:
      - 2
      - 0
    .max_flat_workgroup_size: 512
    .name:           _Z11gemm_kernelPKfPKDF16bS0_Pf
    .private_segment_fixed_size: 0
    .sgpr_count:     30
    .sgpr_spill_count: 0
    .symbol:         _Z11gemm_kernelPKfPKDF16bS0_Pf.kd
    .uniform_work_group_size: 1
    .uses_dynamic_stack: false
    .vgpr_count:     256
    .vgpr_spill_count: 0
    .wavefront_size: 64
